# PEER gather u pass: expert-id ds_bpermutes issued in two bursts instead of one exposed LDS round trip per group (on top of v35)
# speedup vs baseline: 1.0100x; 1.0013x over previous
.LBB0_1138:
	v_and_b32_e32 v4, 15, v148
	v_cmp_eq_u32_e32 vcc, 0, v4
	v_lshlrev_b32_e32 v5, 5, v40
	v_add_u32_e32 v10, 0x80, v148
	v_cndmask_b32_e32 v10, v10, v5, vcc
	v_cmp_gt_u32_e64 s[6:7], 8, v4
	v_lshl_add_u32 v32, v10, 2, v111
	v_and_b32_e32 v36, 12, v148
	v_cndmask_b32_e64 v10, 0, v252, s[6:7]
	v_cmp_lt_u32_e64 s[6:7], 3, v4
	v_lshl_or_b32 v4, v41, 3, v5
	v_add_u32_e32 v34, 0x400, v4
	v_lshlrev_b32_e32 v4, 4, v41
	v_lshl_or_b32 v35, v40, 6, v4
	ds_bpermute_b32 v4, v36, v130
	v_cmp_eq_u32_e32 vcc, 3, v41
	v_cmp_eq_u32_e64 s[2:3], 2, v41
	v_cmp_eq_u32_e64 s[4:5], 1, v41
	v_lshlrev_b32_e32 v129, 4, v148
	s_waitcnt lgkmcnt(0)
	v_mul_lo_u32 v4, v4, s43
	v_add_u32_e32 v5, v4, v35
	v_add_u32_e32 v4, v4, v34
	buffer_load_dwordx4 v[38:41], v5, s[44:47], 0 offen
	buffer_load_dwordx2 v[42:43], v4, s[44:47], 0 offen
	buffer_load_dwordx4 v[44:47], v5, s[44:47], s21 offen
	buffer_load_dwordx2 v[48:49], v4, s[44:47], s33 offen
	buffer_load_dwordx4 v[50:53], v5, s[44:47], s20 offen
	buffer_load_dwordx2 v[54:55], v4, s[44:47], s21 offen
	buffer_load_dwordx4 v[56:59], v5, s[44:47], s23 offen
	buffer_load_dwordx2 v[60:61], v4, s[44:47], s94 offen
	s_mov_b32 s0, 0
	v_cndmask_b32_e64 v33, 1.0, v10, s[6:7]
	ds_bpermute_b32 v222, v36, v130 offset:32
	ds_bpermute_b32 v223, v36, v130 offset:48
	ds_bpermute_b32 v224, v36, v130 offset:64
	ds_bpermute_b32 v225, v36, v130 offset:80
	ds_bpermute_b32 v226, v36, v130 offset:96
	ds_bpermute_b32 v227, v36, v130 offset:112
	ds_bpermute_b32 v228, v36, v130 offset:128
	ds_bpermute_b32 v229, v36, v130 offset:144
	ds_bpermute_b32 v230, v36, v130 offset:160
	ds_bpermute_b32 v231, v36, v130 offset:176
	ds_bpermute_b32 v232, v36, v130 offset:192
	ds_bpermute_b32 v233, v36, v130 offset:208
	ds_bpermute_b32 v234, v36, v130 offset:224
	ds_bpermute_b32 v235, v36, v130 offset:240
	ds_bpermute_b32 v4, v36, v130 offset:16
	s_waitcnt lgkmcnt(0)
	v_mul_lo_u32 v4, v4, s43
	v_add_u32_e32 v5, v4, v35
	v_add_u32_e32 v4, v4, v34
	buffer_load_dwordx4 v[62:65], v5, s[44:47], 0 offen
	buffer_load_dwordx4 v[68:71], v5, s[44:47], s20 offen
	buffer_load_dwordx4 v[74:77], v5, s[44:47], s21 offen
	buffer_load_dwordx4 v[86:89], v5, s[44:47], s23 offen
	buffer_load_dwordx2 v[66:67], v4, s[44:47], 0 offen
	buffer_load_dwordx2 v[78:79], v4, s[44:47], s33 offen
	buffer_load_dwordx2 v[72:73], v4, s[44:47], s21 offen
	buffer_load_dwordx2 v[90:91], v4, s[44:47], s94 offen
	v_mul_lo_u32 v4, v222, s43
	v_add_u32_e32 v5, v4, v35
	v_add_u32_e32 v4, v4, v34
	buffer_load_dwordx4 v[92:95], v5, s[44:47], 0 offen
	buffer_load_dwordx4 v[98:101], v5, s[44:47], s20 offen
	buffer_load_dwordx4 v[150:153], v5, s[44:47], s21 offen
	buffer_load_dwordx4 v[156:159], v5, s[44:47], s23 offen
	buffer_load_dwordx2 v[96:97], v4, s[44:47], 0 offen
	buffer_load_dwordx2 v[154:155], v4, s[44:47], s33 offen
	buffer_load_dwordx2 v[102:103], v4, s[44:47], s21 offen
	buffer_load_dwordx2 v[160:161], v4, s[44:47], s94 offen
	v_mul_lo_u32 v4, v223, s43
	v_add_u32_e32 v5, v4, v35
	v_add_u32_e32 v4, v4, v34
	buffer_load_dwordx4 v[162:165], v5, s[44:47], 0 offen
	buffer_load_dwordx4 v[168:171], v5, s[44:47], s20 offen
	buffer_load_dwordx4 v[174:177], v5, s[44:47], s21 offen
	buffer_load_dwordx4 v[216:219], v5, s[44:47], s23 offen
	buffer_load_dwordx2 v[166:167], v4, s[44:47], 0 offen
	buffer_load_dwordx2 v[178:179], v4, s[44:47], s33 offen
	buffer_load_dwordx2 v[172:173], v4, s[44:47], s21 offen
	buffer_load_dwordx2 v[220:221], v4, s[44:47], s94 offen
	v_mov_b32_e32 v22, v28
	v_mov_b32_e32 v23, v29
	v_mov_b32_e32 v16, v30
	v_mov_b32_e32 v17, v31
	s_waitcnt vmcnt(30)
	v_mfma_f32_16x16x128_f8f6f4 v[38:41], v[38:43], v[18:23], 0 cbsz:2 blgp:2
	v_mov_b32_e32 v10, v24
	v_mov_b32_e32 v11, v25
	v_mov_b32_e32 v4, v26
	s_waitcnt vmcnt(28)
	v_mfma_f32_16x16x128_f8f6f4 v[28:31], v[44:49], v[12:17], v[38:41] cbsz:2 blgp:2
	v_mov_b32_e32 v5, v27
	s_waitcnt vmcnt(26)
	v_mfma_f32_16x16x128_f8f6f4 v[28:31], v[50:55], v[6:11], v[28:31] cbsz:2 blgp:2
	s_waitcnt vmcnt(24)
	v_mfma_f32_16x16x128_f8f6f4 v[24:27], v[56:61], v[0:5], v[28:31] cbsz:2 blgp:2
	s_nop 7
	v_cndmask_b32_e64 v24, v24, v25, s[4:5]
	v_cndmask_b32_e64 v24, v24, v26, s[2:3]
	v_cndmask_b32_e32 v24, v24, v27, vcc
	v_mul_f32_e32 v25, v33, v24
	s_nop 1
	v_mov_b32_dpp v25, v25 quad_perm:[1,0,3,2] row_mask:0xf bank_mask:0xf bound_ctrl:1
	v_fmac_f32_e32 v25, v33, v24
	s_nop 1
	v_add_f32_dpp v24, v25, v25 quad_perm:[2,3,0,1] row_mask:0xf bank_mask:0xf bound_ctrl:1
	s_nop 1
	v_add_f32_dpp v24, v24, v24 row_half_mirror row_mask:0xf bank_mask:0xf bound_ctrl:1
	ds_write_b32 v32, v24 offset:49152
	v_mul_lo_u32 v24, v224, s43
	v_add_u32_e32 v28, v24, v35
	v_add_u32_e32 v30, v24, v34
	buffer_load_dwordx4 v[24:27], v28, s[44:47], 0 offen
	buffer_load_dwordx4 v[38:41], v28, s[44:47], s20 offen
	buffer_load_dwordx4 v[44:47], v28, s[44:47], s21 offen
	buffer_load_dwordx4 v[50:53], v28, s[44:47], s23 offen
	s_nop 0
	buffer_load_dwordx2 v[28:29], v30, s[44:47], 0 offen
	buffer_load_dwordx2 v[48:49], v30, s[44:47], s33 offen
	buffer_load_dwordx2 v[42:43], v30, s[44:47], s21 offen
	buffer_load_dwordx2 v[54:55], v30, s[44:47], s94 offen
	s_waitcnt vmcnt(27)
	v_mfma_f32_16x16x128_f8f6f4 v[56:59], v[62:67], v[18:23], 0 cbsz:2 blgp:2
	s_waitcnt vmcnt(26)
	v_mfma_f32_16x16x128_f8f6f4 v[56:59], v[74:79], v[12:17], v[56:59] cbsz:2 blgp:2
	s_waitcnt vmcnt(25)
	v_mfma_f32_16x16x128_f8f6f4 v[56:59], v[68:73], v[6:11], v[56:59] cbsz:2 blgp:2
	s_waitcnt vmcnt(24)
	v_mfma_f32_16x16x128_f8f6f4 v[56:59], v[86:91], v[0:5], v[56:59] cbsz:2 blgp:2
	s_nop 7
	v_cndmask_b32_e64 v30, v56, v57, s[4:5]
	v_cndmask_b32_e64 v30, v30, v58, s[2:3]
	v_cndmask_b32_e32 v30, v30, v59, vcc
	v_mul_f32_e32 v31, v33, v30
	s_nop 1
	v_mov_b32_dpp v31, v31 quad_perm:[1,0,3,2] row_mask:0xf bank_mask:0xf bound_ctrl:1
	v_fmac_f32_e32 v31, v33, v30
	s_nop 1
	v_add_f32_dpp v30, v31, v31 quad_perm:[2,3,0,1] row_mask:0xf bank_mask:0xf bound_ctrl:1
	s_nop 1
	v_add_f32_dpp v30, v30, v30 row_half_mirror row_mask:0xf bank_mask:0xf bound_ctrl:1
	ds_write_b32 v32, v30 offset:49156
	v_mul_lo_u32 v30, v225, s43
	v_add_u32_e32 v31, v30, v35
	v_add_u32_e32 v30, v30, v34
	buffer_load_dwordx4 v[56:59], v31, s[44:47], 0 offen
	buffer_load_dwordx4 v[62:65], v31, s[44:47], s20 offen
	buffer_load_dwordx4 v[68:71], v31, s[44:47], s21 offen
	buffer_load_dwordx4 v[74:77], v31, s[44:47], s23 offen
	buffer_load_dwordx2 v[60:61], v30, s[44:47], 0 offen
	buffer_load_dwordx2 v[72:73], v30, s[44:47], s33 offen
	buffer_load_dwordx2 v[66:67], v30, s[44:47], s21 offen
	buffer_load_dwordx2 v[78:79], v30, s[44:47], s94 offen
	s_waitcnt vmcnt(27)
	v_mfma_f32_16x16x128_f8f6f4 v[86:89], v[92:97], v[18:23], 0 cbsz:2 blgp:2
	s_waitcnt vmcnt(26)
	v_mfma_f32_16x16x128_f8f6f4 v[86:89], v[150:155], v[12:17], v[86:89] cbsz:2 blgp:2
	s_waitcnt vmcnt(25)
	v_mfma_f32_16x16x128_f8f6f4 v[86:89], v[98:103], v[6:11], v[86:89] cbsz:2 blgp:2
	s_waitcnt vmcnt(24)
	v_mfma_f32_16x16x128_f8f6f4 v[86:89], v[156:161], v[0:5], v[86:89] cbsz:2 blgp:2
	s_nop 7
	v_cndmask_b32_e64 v30, v86, v87, s[4:5]
	v_cndmask_b32_e64 v30, v30, v88, s[2:3]
	v_cndmask_b32_e32 v30, v30, v89, vcc
	v_mul_f32_e32 v31, v33, v30
	s_nop 1
	v_mov_b32_dpp v31, v31 quad_perm:[1,0,3,2] row_mask:0xf bank_mask:0xf bound_ctrl:1
	v_fmac_f32_e32 v31, v33, v30
	s_nop 1
	v_add_f32_dpp v30, v31, v31 quad_perm:[2,3,0,1] row_mask:0xf bank_mask:0xf bound_ctrl:1
	s_nop 1
	v_add_f32_dpp v30, v30, v30 row_half_mirror row_mask:0xf bank_mask:0xf bound_ctrl:1
	ds_write_b32 v32, v30 offset:49160
	v_mul_lo_u32 v30, v226, s43
	v_add_u32_e32 v31, v30, v35
	v_add_u32_e32 v30, v30, v34
	buffer_load_dwordx4 v[86:89], v31, s[44:47], 0 offen
	buffer_load_dwordx4 v[92:95], v31, s[44:47], s20 offen
	buffer_load_dwordx4 v[98:101], v31, s[44:47], s21 offen
	buffer_load_dwordx4 v[150:153], v31, s[44:47], s23 offen
	buffer_load_dwordx2 v[90:91], v30, s[44:47], 0 offen
	buffer_load_dwordx2 v[102:103], v30, s[44:47], s33 offen
	buffer_load_dwordx2 v[96:97], v30, s[44:47], s21 offen
	buffer_load_dwordx2 v[154:155], v30, s[44:47], s94 offen
	s_waitcnt vmcnt(27)
	v_mfma_f32_16x16x128_f8f6f4 v[156:159], v[162:167], v[18:23], 0 cbsz:2 blgp:2
	s_waitcnt vmcnt(26)
	v_mfma_f32_16x16x128_f8f6f4 v[156:159], v[174:179], v[12:17], v[156:159] cbsz:2 blgp:2
	s_waitcnt vmcnt(25)
	v_mfma_f32_16x16x128_f8f6f4 v[156:159], v[168:173], v[6:11], v[156:159] cbsz:2 blgp:2
	s_waitcnt vmcnt(24)
	v_mfma_f32_16x16x128_f8f6f4 v[156:159], v[216:221], v[0:5], v[156:159] cbsz:2 blgp:2
	s_nop 7
	v_cndmask_b32_e64 v30, v156, v157, s[4:5]
	v_cndmask_b32_e64 v30, v30, v158, s[2:3]
	v_cndmask_b32_e32 v30, v30, v159, vcc
	v_mul_f32_e32 v31, v33, v30
	s_nop 1
	v_mov_b32_dpp v31, v31 quad_perm:[1,0,3,2] row_mask:0xf bank_mask:0xf bound_ctrl:1
	v_fmac_f32_e32 v31, v33, v30
	s_nop 1
	v_add_f32_dpp v30, v31, v31 quad_perm:[2,3,0,1] row_mask:0xf bank_mask:0xf bound_ctrl:1
	s_nop 1
	v_add_f32_dpp v30, v30, v30 row_half_mirror row_mask:0xf bank_mask:0xf bound_ctrl:1
	ds_write_b32 v32, v30 offset:49164
	v_mul_lo_u32 v30, v227, s43
	v_add_u32_e32 v31, v30, v35
	v_add_u32_e32 v30, v30, v34
	buffer_load_dwordx4 v[156:159], v31, s[44:47], 0 offen
	buffer_load_dwordx4 v[162:165], v31, s[44:47], s20 offen
	buffer_load_dwordx4 v[168:171], v31, s[44:47], s21 offen
	buffer_load_dwordx4 v[174:177], v31, s[44:47], s23 offen
	buffer_load_dwordx2 v[160:161], v30, s[44:47], 0 offen
	buffer_load_dwordx2 v[172:173], v30, s[44:47], s33 offen
	buffer_load_dwordx2 v[166:167], v30, s[44:47], s21 offen
	buffer_load_dwordx2 v[178:179], v30, s[44:47], s94 offen
	s_waitcnt vmcnt(27)
	v_mfma_f32_16x16x128_f8f6f4 v[24:27], v[24:29], v[18:23], 0 cbsz:2 blgp:2
	s_waitcnt vmcnt(26)
	v_mfma_f32_16x16x128_f8f6f4 v[24:27], v[44:49], v[12:17], v[24:27] cbsz:2 blgp:2
	s_waitcnt vmcnt(25)
	v_mfma_f32_16x16x128_f8f6f4 v[24:27], v[38:43], v[6:11], v[24:27] cbsz:2 blgp:2
	s_waitcnt vmcnt(24)
	v_mfma_f32_16x16x128_f8f6f4 v[24:27], v[50:55], v[0:5], v[24:27] cbsz:2 blgp:2
	s_nop 7
	v_cndmask_b32_e64 v24, v24, v25, s[4:5]
	v_cndmask_b32_e64 v24, v24, v26, s[2:3]
	v_cndmask_b32_e32 v24, v24, v27, vcc
	v_mul_f32_e32 v25, v33, v24
	s_nop 1
	v_mov_b32_dpp v25, v25 quad_perm:[1,0,3,2] row_mask:0xf bank_mask:0xf bound_ctrl:1
	v_fmac_f32_e32 v25, v33, v24
	s_nop 1
	v_add_f32_dpp v24, v25, v25 quad_perm:[2,3,0,1] row_mask:0xf bank_mask:0xf bound_ctrl:1
	s_nop 1
	v_add_f32_dpp v24, v24, v24 row_half_mirror row_mask:0xf bank_mask:0xf bound_ctrl:1
	ds_write_b32 v32, v24 offset:49168
	v_mul_lo_u32 v24, v228, s43
	v_add_u32_e32 v28, v24, v35
	v_add_u32_e32 v30, v24, v34
	buffer_load_dwordx4 v[24:27], v28, s[44:47], 0 offen
	buffer_load_dwordx4 v[38:41], v28, s[44:47], s20 offen
	buffer_load_dwordx4 v[44:47], v28, s[44:47], s21 offen
	buffer_load_dwordx4 v[50:53], v28, s[44:47], s23 offen
	s_nop 0
	buffer_load_dwordx2 v[28:29], v30, s[44:47], 0 offen
	buffer_load_dwordx2 v[48:49], v30, s[44:47], s33 offen
	buffer_load_dwordx2 v[42:43], v30, s[44:47], s21 offen
	buffer_load_dwordx2 v[54:55], v30, s[44:47], s94 offen
	s_waitcnt vmcnt(27)
	v_mfma_f32_16x16x128_f8f6f4 v[56:59], v[56:61], v[18:23], 0 cbsz:2 blgp:2
	s_waitcnt vmcnt(26)
	v_mfma_f32_16x16x128_f8f6f4 v[56:59], v[68:73], v[12:17], v[56:59] cbsz:2 blgp:2
	s_waitcnt vmcnt(25)
	v_mfma_f32_16x16x128_f8f6f4 v[56:59], v[62:67], v[6:11], v[56:59] cbsz:2 blgp:2
	s_waitcnt vmcnt(24)
	v_mfma_f32_16x16x128_f8f6f4 v[56:59], v[74:79], v[0:5], v[56:59] cbsz:2 blgp:2
	s_nop 7
	v_cndmask_b32_e64 v30, v56, v57, s[4:5]
	v_cndmask_b32_e64 v30, v30, v58, s[2:3]
	v_cndmask_b32_e32 v30, v30, v59, vcc
	v_mul_f32_e32 v31, v33, v30
	s_nop 1
	v_mov_b32_dpp v31, v31 quad_perm:[1,0,3,2] row_mask:0xf bank_mask:0xf bound_ctrl:1
	v_fmac_f32_e32 v31, v33, v30
	s_nop 1
	v_add_f32_dpp v30, v31, v31 quad_perm:[2,3,0,1] row_mask:0xf bank_mask:0xf bound_ctrl:1
	s_nop 1
	v_add_f32_dpp v30, v30, v30 row_half_mirror row_mask:0xf bank_mask:0xf bound_ctrl:1
	ds_write_b32 v32, v30 offset:49172
	v_mul_lo_u32 v30, v229, s43
	v_add_u32_e32 v31, v30, v35
	v_add_u32_e32 v30, v30, v34
	buffer_load_dwordx4 v[56:59], v31, s[44:47], 0 offen
	buffer_load_dwordx4 v[62:65], v31, s[44:47], s20 offen
	buffer_load_dwordx4 v[68:71], v31, s[44:47], s21 offen
	buffer_load_dwordx4 v[74:77], v31, s[44:47], s23 offen
	buffer_load_dwordx2 v[60:61], v30, s[44:47], 0 offen
	buffer_load_dwordx2 v[72:73], v30, s[44:47], s33 offen
	buffer_load_dwordx2 v[66:67], v30, s[44:47], s21 offen
	buffer_load_dwordx2 v[78:79], v30, s[44:47], s94 offen
	s_waitcnt vmcnt(27)
	v_mfma_f32_16x16x128_f8f6f4 v[86:89], v[86:91], v[18:23], 0 cbsz:2 blgp:2
	s_waitcnt vmcnt(26)
	v_mfma_f32_16x16x128_f8f6f4 v[86:89], v[98:103], v[12:17], v[86:89] cbsz:2 blgp:2
	s_waitcnt vmcnt(25)
	v_mfma_f32_16x16x128_f8f6f4 v[86:89], v[92:97], v[6:11], v[86:89] cbsz:2 blgp:2
	s_waitcnt vmcnt(24)
	v_mfma_f32_16x16x128_f8f6f4 v[86:89], v[150:155], v[0:5], v[86:89] cbsz:2 blgp:2
	s_nop 7
	v_cndmask_b32_e64 v30, v86, v87, s[4:5]
	v_cndmask_b32_e64 v30, v30, v88, s[2:3]
	v_cndmask_b32_e32 v30, v30, v89, vcc
	v_mul_f32_e32 v31, v33, v30
	s_nop 1
	v_mov_b32_dpp v31, v31 quad_perm:[1,0,3,2] row_mask:0xf bank_mask:0xf bound_ctrl:1
	v_fmac_f32_e32 v31, v33, v30
	s_nop 1
	v_add_f32_dpp v30, v31, v31 quad_perm:[2,3,0,1] row_mask:0xf bank_mask:0xf bound_ctrl:1
	s_nop 1
	v_add_f32_dpp v30, v30, v30 row_half_mirror row_mask:0xf bank_mask:0xf bound_ctrl:1
	ds_write_b32 v32, v30 offset:49176
	v_mul_lo_u32 v30, v230, s43
	v_add_u32_e32 v31, v30, v35
	v_add_u32_e32 v30, v30, v34
	buffer_load_dwordx4 v[86:89], v31, s[44:47], 0 offen
	buffer_load_dwordx4 v[92:95], v31, s[44:47], s20 offen
	buffer_load_dwordx4 v[98:101], v31, s[44:47], s21 offen
	buffer_load_dwordx4 v[150:153], v31, s[44:47], s23 offen
	buffer_load_dwordx2 v[90:91], v30, s[44:47], 0 offen
	buffer_load_dwordx2 v[102:103], v30, s[44:47], s33 offen
	buffer_load_dwordx2 v[96:97], v30, s[44:47], s21 offen
	buffer_load_dwordx2 v[154:155], v30, s[44:47], s94 offen
	s_waitcnt vmcnt(27)
	v_mfma_f32_16x16x128_f8f6f4 v[156:159], v[156:161], v[18:23], 0 cbsz:2 blgp:2
	s_waitcnt vmcnt(26)
	v_mfma_f32_16x16x128_f8f6f4 v[156:159], v[168:173], v[12:17], v[156:159] cbsz:2 blgp:2
	s_waitcnt vmcnt(25)
	v_mfma_f32_16x16x128_f8f6f4 v[156:159], v[162:167], v[6:11], v[156:159] cbsz:2 blgp:2
	s_waitcnt vmcnt(24)
	v_mfma_f32_16x16x128_f8f6f4 v[156:159], v[174:179], v[0:5], v[156:159] cbsz:2 blgp:2
	s_nop 7
	v_cndmask_b32_e64 v30, v156, v157, s[4:5]
	v_cndmask_b32_e64 v30, v30, v158, s[2:3]
	v_cndmask_b32_e32 v30, v30, v159, vcc
	v_mul_f32_e32 v31, v33, v30
	s_nop 1
	v_mov_b32_dpp v31, v31 quad_perm:[1,0,3,2] row_mask:0xf bank_mask:0xf bound_ctrl:1
	v_fmac_f32_e32 v31, v33, v30
	s_nop 1
	v_add_f32_dpp v30, v31, v31 quad_perm:[2,3,0,1] row_mask:0xf bank_mask:0xf bound_ctrl:1
	s_nop 1
	v_add_f32_dpp v30, v30, v30 row_half_mirror row_mask:0xf bank_mask:0xf bound_ctrl:1
	ds_write_b32 v32, v30 offset:49180
	v_mul_lo_u32 v30, v231, s43
	v_add_u32_e32 v31, v30, v35
	v_add_u32_e32 v30, v30, v34
	buffer_load_dwordx4 v[156:159], v31, s[44:47], 0 offen
	buffer_load_dwordx4 v[162:165], v31, s[44:47], s20 offen
	buffer_load_dwordx4 v[168:171], v31, s[44:47], s21 offen
	buffer_load_dwordx4 v[174:177], v31, s[44:47], s23 offen
	buffer_load_dwordx2 v[160:161], v30, s[44:47], 0 offen
	buffer_load_dwordx2 v[172:173], v30, s[44:47], s33 offen
	buffer_load_dwordx2 v[166:167], v30, s[44:47], s21 offen
	buffer_load_dwordx2 v[178:179], v30, s[44:47], s94 offen
	s_waitcnt vmcnt(27)
	v_mfma_f32_16x16x128_f8f6f4 v[24:27], v[24:29], v[18:23], 0 cbsz:2 blgp:2
	s_waitcnt vmcnt(26)
	v_mfma_f32_16x16x128_f8f6f4 v[24:27], v[44:49], v[12:17], v[24:27] cbsz:2 blgp:2
	s_waitcnt vmcnt(25)
	v_mfma_f32_16x16x128_f8f6f4 v[24:27], v[38:43], v[6:11], v[24:27] cbsz:2 blgp:2
	s_waitcnt vmcnt(24)
	v_mfma_f32_16x16x128_f8f6f4 v[24:27], v[50:55], v[0:5], v[24:27] cbsz:2 blgp:2
	s_nop 7
	v_cndmask_b32_e64 v24, v24, v25, s[4:5]
	v_cndmask_b32_e64 v24, v24, v26, s[2:3]
	v_cndmask_b32_e32 v24, v24, v27, vcc
	v_mul_f32_e32 v25, v33, v24
	s_nop 1
	v_mov_b32_dpp v25, v25 quad_perm:[1,0,3,2] row_mask:0xf bank_mask:0xf bound_ctrl:1
	v_fmac_f32_e32 v25, v33, v24
	s_nop 1
	v_add_f32_dpp v24, v25, v25 quad_perm:[2,3,0,1] row_mask:0xf bank_mask:0xf bound_ctrl:1
	s_nop 1
	v_add_f32_dpp v24, v24, v24 row_half_mirror row_mask:0xf bank_mask:0xf bound_ctrl:1
	ds_write_b32 v32, v24 offset:49184
	v_mul_lo_u32 v24, v232, s43
	v_add_u32_e32 v28, v24, v35
	v_add_u32_e32 v30, v24, v34
	buffer_load_dwordx4 v[24:27], v28, s[44:47], 0 offen
	buffer_load_dwordx4 v[38:41], v28, s[44:47], s20 offen
	buffer_load_dwordx4 v[44:47], v28, s[44:47], s21 offen
	buffer_load_dwordx4 v[50:53], v28, s[44:47], s23 offen
	s_nop 0
	buffer_load_dwordx2 v[28:29], v30, s[44:47], 0 offen
	buffer_load_dwordx2 v[48:49], v30, s[44:47], s33 offen
	buffer_load_dwordx2 v[42:43], v30, s[44:47], s21 offen
	buffer_load_dwordx2 v[54:55], v30, s[44:47], s94 offen
	s_waitcnt vmcnt(27)
	v_mfma_f32_16x16x128_f8f6f4 v[56:59], v[56:61], v[18:23], 0 cbsz:2 blgp:2
	s_waitcnt vmcnt(26)
	v_mfma_f32_16x16x128_f8f6f4 v[56:59], v[68:73], v[12:17], v[56:59] cbsz:2 blgp:2
	s_waitcnt vmcnt(25)
	v_mfma_f32_16x16x128_f8f6f4 v[56:59], v[62:67], v[6:11], v[56:59] cbsz:2 blgp:2
	s_waitcnt vmcnt(24)
	v_mfma_f32_16x16x128_f8f6f4 v[56:59], v[74:79], v[0:5], v[56:59] cbsz:2 blgp:2
	s_nop 7
	v_cndmask_b32_e64 v30, v56, v57, s[4:5]
	v_cndmask_b32_e64 v30, v30, v58, s[2:3]
	v_cndmask_b32_e32 v30, v30, v59, vcc
	v_mul_f32_e32 v31, v33, v30
	s_nop 1
	v_mov_b32_dpp v31, v31 quad_perm:[1,0,3,2] row_mask:0xf bank_mask:0xf bound_ctrl:1
	v_fmac_f32_e32 v31, v33, v30
	s_nop 1
	v_add_f32_dpp v30, v31, v31 quad_perm:[2,3,0,1] row_mask:0xf bank_mask:0xf bound_ctrl:1
	s_nop 1
	v_add_f32_dpp v30, v30, v30 row_half_mirror row_mask:0xf bank_mask:0xf bound_ctrl:1
	ds_write_b32 v32, v30 offset:49188
	v_mul_lo_u32 v30, v233, s43
	v_add_u32_e32 v31, v30, v35
	v_add_u32_e32 v30, v30, v34
	buffer_load_dwordx4 v[56:59], v31, s[44:47], 0 offen
	buffer_load_dwordx4 v[62:65], v31, s[44:47], s20 offen
	buffer_load_dwordx4 v[68:71], v31, s[44:47], s21 offen
	buffer_load_dwordx4 v[74:77], v31, s[44:47], s23 offen
	buffer_load_dwordx2 v[60:61], v30, s[44:47], 0 offen
	buffer_load_dwordx2 v[72:73], v30, s[44:47], s33 offen
	buffer_load_dwordx2 v[66:67], v30, s[44:47], s21 offen
	buffer_load_dwordx2 v[78:79], v30, s[44:47], s94 offen
	s_waitcnt vmcnt(27)
	v_mfma_f32_16x16x128_f8f6f4 v[86:89], v[86:91], v[18:23], 0 cbsz:2 blgp:2
	s_waitcnt vmcnt(26)
	v_mfma_f32_16x16x128_f8f6f4 v[86:89], v[98:103], v[12:17], v[86:89] cbsz:2 blgp:2
	s_waitcnt vmcnt(25)
	v_mfma_f32_16x16x128_f8f6f4 v[86:89], v[92:97], v[6:11], v[86:89] cbsz:2 blgp:2
	s_waitcnt vmcnt(24)
	v_mfma_f32_16x16x128_f8f6f4 v[86:89], v[150:155], v[0:5], v[86:89] cbsz:2 blgp:2
	s_nop 7
	v_cndmask_b32_e64 v30, v86, v87, s[4:5]
	v_cndmask_b32_e64 v30, v30, v88, s[2:3]
	v_cndmask_b32_e32 v30, v30, v89, vcc
	v_mul_f32_e32 v31, v33, v30
	s_nop 1
	v_mov_b32_dpp v31, v31 quad_perm:[1,0,3,2] row_mask:0xf bank_mask:0xf bound_ctrl:1
	v_fmac_f32_e32 v31, v33, v30
	s_nop 1
	v_add_f32_dpp v30, v31, v31 quad_perm:[2,3,0,1] row_mask:0xf bank_mask:0xf bound_ctrl:1
	s_nop 1
	v_add_f32_dpp v30, v30, v30 row_half_mirror row_mask:0xf bank_mask:0xf bound_ctrl:1
	ds_write_b32 v32, v30 offset:49192
	v_mul_lo_u32 v30, v234, s43
	v_add_u32_e32 v31, v30, v35
	v_add_u32_e32 v30, v30, v34
	buffer_load_dwordx4 v[86:89], v31, s[44:47], 0 offen
	buffer_load_dwordx4 v[92:95], v31, s[44:47], s20 offen
	buffer_load_dwordx4 v[98:101], v31, s[44:47], s21 offen
	buffer_load_dwordx4 v[150:153], v31, s[44:47], s23 offen
	buffer_load_dwordx2 v[90:91], v30, s[44:47], 0 offen
	buffer_load_dwordx2 v[102:103], v30, s[44:47], s33 offen
	buffer_load_dwordx2 v[96:97], v30, s[44:47], s21 offen
	buffer_load_dwordx2 v[154:155], v30, s[44:47], s94 offen
	s_waitcnt vmcnt(27)
	v_mfma_f32_16x16x128_f8f6f4 v[156:159], v[156:161], v[18:23], 0 cbsz:2 blgp:2
	s_waitcnt vmcnt(26)
	v_mfma_f32_16x16x128_f8f6f4 v[156:159], v[168:173], v[12:17], v[156:159] cbsz:2 blgp:2
	s_waitcnt vmcnt(25)
	v_mfma_f32_16x16x128_f8f6f4 v[156:159], v[162:167], v[6:11], v[156:159] cbsz:2 blgp:2
	s_waitcnt vmcnt(24)
	v_mfma_f32_16x16x128_f8f6f4 v[156:159], v[174:179], v[0:5], v[156:159] cbsz:2 blgp:2
	s_nop 7
	v_cndmask_b32_e64 v30, v156, v157, s[4:5]
	v_cndmask_b32_e64 v30, v30, v158, s[2:3]
	v_cndmask_b32_e32 v30, v30, v159, vcc
	v_mul_f32_e32 v31, v33, v30
	s_nop 1
	v_mov_b32_dpp v31, v31 quad_perm:[1,0,3,2] row_mask:0xf bank_mask:0xf bound_ctrl:1
	v_fmac_f32_e32 v31, v33, v30
	s_nop 1
	v_add_f32_dpp v30, v31, v31 quad_perm:[2,3,0,1] row_mask:0xf bank_mask:0xf bound_ctrl:1
	s_nop 1
	v_add_f32_dpp v30, v30, v30 row_half_mirror row_mask:0xf bank_mask:0xf bound_ctrl:1
	ds_write_b32 v32, v30 offset:49196
	v_mul_lo_u32 v30, v235, s43
	v_add_u32_e32 v31, v30, v35
	v_add_u32_e32 v30, v30, v34
	buffer_load_dwordx4 v[156:159], v31, s[44:47], 0 offen
	buffer_load_dwordx4 v[162:165], v31, s[44:47], s20 offen
	buffer_load_dwordx4 v[168:171], v31, s[44:47], s21 offen
	buffer_load_dwordx4 v[174:177], v31, s[44:47], s23 offen
	buffer_load_dwordx2 v[160:161], v30, s[44:47], 0 offen
	buffer_load_dwordx2 v[172:173], v30, s[44:47], s33 offen
	buffer_load_dwordx2 v[166:167], v30, s[44:47], s21 offen
	buffer_load_dwordx2 v[178:179], v30, s[44:47], s94 offen
	s_waitcnt vmcnt(27)
	v_mfma_f32_16x16x128_f8f6f4 v[24:27], v[24:29], v[18:23], 0 cbsz:2 blgp:2
	s_waitcnt vmcnt(26)
	v_mfma_f32_16x16x128_f8f6f4 v[24:27], v[44:49], v[12:17], v[24:27] cbsz:2 blgp:2
	s_waitcnt vmcnt(25)
	v_mfma_f32_16x16x128_f8f6f4 v[24:27], v[38:43], v[6:11], v[24:27] cbsz:2 blgp:2
	s_waitcnt vmcnt(24)
	v_mfma_f32_16x16x128_f8f6f4 v[24:27], v[50:55], v[0:5], v[24:27] cbsz:2 blgp:2
	s_nop 7
	v_cndmask_b32_e64 v24, v24, v25, s[4:5]
	v_cndmask_b32_e64 v24, v24, v26, s[2:3]
	v_cndmask_b32_e32 v24, v24, v27, vcc
	v_mul_f32_e32 v25, v33, v24
	s_nop 1
	v_mov_b32_dpp v25, v25 quad_perm:[1,0,3,2] row_mask:0xf bank_mask:0xf bound_ctrl:1
	v_fmac_f32_e32 v25, v33, v24
	s_nop 1
	v_add_f32_dpp v24, v25, v25 quad_perm:[2,3,0,1] row_mask:0xf bank_mask:0xf bound_ctrl:1
	s_nop 1
	v_add_f32_dpp v24, v24, v24 row_half_mirror row_mask:0xf bank_mask:0xf bound_ctrl:1
	ds_write_b32 v32, v24 offset:49200
	ds_bpermute_b32 v236, v36, v128 offset:16
	ds_bpermute_b32 v237, v36, v128 offset:32
	ds_bpermute_b32 v238, v36, v128 offset:48
	ds_bpermute_b32 v239, v36, v128 offset:64
	ds_bpermute_b32 v240, v36, v128 offset:80
	ds_bpermute_b32 v241, v36, v128 offset:96
	ds_bpermute_b32 v242, v36, v128 offset:112
	ds_bpermute_b32 v243, v36, v128 offset:128
	ds_bpermute_b32 v244, v36, v128 offset:144
	ds_bpermute_b32 v245, v36, v128 offset:160
	ds_bpermute_b32 v246, v36, v128 offset:176
	ds_bpermute_b32 v247, v36, v128 offset:192
	ds_bpermute_b32 v248, v36, v128 offset:208
	ds_bpermute_b32 v249, v36, v128 offset:224
	ds_bpermute_b32 v24, v36, v128
	s_waitcnt lgkmcnt(0)
	v_mul_lo_u32 v24, v24, s43
	v_add_u32_e32 v28, v24, v35
	v_add_u32_e32 v30, v24, v34
	buffer_load_dwordx4 v[24:27], v28, s[44:47], 0 offen
	buffer_load_dwordx4 v[38:41], v28, s[44:47], s20 offen
	buffer_load_dwordx4 v[44:47], v28, s[44:47], s21 offen
	buffer_load_dwordx4 v[50:53], v28, s[44:47], s23 offen
	s_nop 0
	buffer_load_dwordx2 v[28:29], v30, s[44:47], 0 offen
	buffer_load_dwordx2 v[48:49], v30, s[44:47], s33 offen
	buffer_load_dwordx2 v[42:43], v30, s[44:47], s21 offen
	buffer_load_dwordx2 v[54:55], v30, s[44:47], s94 offen
	s_waitcnt vmcnt(27)
	v_mfma_f32_16x16x128_f8f6f4 v[56:59], v[56:61], v[18:23], 0 cbsz:2 blgp:2
	s_waitcnt vmcnt(26)
	v_mfma_f32_16x16x128_f8f6f4 v[56:59], v[68:73], v[12:17], v[56:59] cbsz:2 blgp:2
	s_waitcnt vmcnt(25)
	v_mfma_f32_16x16x128_f8f6f4 v[56:59], v[62:67], v[6:11], v[56:59] cbsz:2 blgp:2
	s_waitcnt vmcnt(24)
	v_mfma_f32_16x16x128_f8f6f4 v[56:59], v[74:79], v[0:5], v[56:59] cbsz:2 blgp:2
	s_nop 7
	v_cndmask_b32_e64 v30, v56, v57, s[4:5]
	v_cndmask_b32_e64 v30, v30, v58, s[2:3]
	v_cndmask_b32_e32 v30, v30, v59, vcc
	v_mul_f32_e32 v31, v33, v30
	s_nop 1
	v_mov_b32_dpp v31, v31 quad_perm:[1,0,3,2] row_mask:0xf bank_mask:0xf bound_ctrl:1
	v_fmac_f32_e32 v31, v33, v30
	s_nop 1
	v_add_f32_dpp v30, v31, v31 quad_perm:[2,3,0,1] row_mask:0xf bank_mask:0xf bound_ctrl:1
	s_nop 1
	v_add_f32_dpp v30, v30, v30 row_half_mirror row_mask:0xf bank_mask:0xf bound_ctrl:1
	ds_write_b32 v32, v30 offset:49204
	v_mul_lo_u32 v30, v236, s43
	v_add_u32_e32 v31, v30, v35
	v_add_u32_e32 v30, v30, v34
	buffer_load_dwordx4 v[56:59], v31, s[44:47], 0 offen
	buffer_load_dwordx4 v[62:65], v31, s[44:47], s20 offen
	buffer_load_dwordx4 v[68:71], v31, s[44:47], s21 offen
	buffer_load_dwordx4 v[74:77], v31, s[44:47], s23 offen
	buffer_load_dwordx2 v[60:61], v30, s[44:47], 0 offen
	buffer_load_dwordx2 v[72:73], v30, s[44:47], s33 offen
	buffer_load_dwordx2 v[66:67], v30, s[44:47], s21 offen
	buffer_load_dwordx2 v[78:79], v30, s[44:47], s94 offen
	s_waitcnt vmcnt(27)
	v_mfma_f32_16x16x128_f8f6f4 v[86:89], v[86:91], v[18:23], 0 cbsz:2 blgp:2
	s_waitcnt vmcnt(26)
	v_mfma_f32_16x16x128_f8f6f4 v[86:89], v[98:103], v[12:17], v[86:89] cbsz:2 blgp:2
	s_waitcnt vmcnt(25)
	v_mfma_f32_16x16x128_f8f6f4 v[86:89], v[92:97], v[6:11], v[86:89] cbsz:2 blgp:2
	s_waitcnt vmcnt(24)
	v_mfma_f32_16x16x128_f8f6f4 v[86:89], v[150:155], v[0:5], v[86:89] cbsz:2 blgp:2
	s_nop 7
	v_cndmask_b32_e64 v30, v86, v87, s[4:5]
	v_cndmask_b32_e64 v30, v30, v88, s[2:3]
	v_cndmask_b32_e32 v30, v30, v89, vcc
	v_mul_f32_e32 v31, v33, v30
	s_nop 1
	v_mov_b32_dpp v31, v31 quad_perm:[1,0,3,2] row_mask:0xf bank_mask:0xf bound_ctrl:1
	v_fmac_f32_e32 v31, v33, v30
	s_nop 1
	v_add_f32_dpp v30, v31, v31 quad_perm:[2,3,0,1] row_mask:0xf bank_mask:0xf bound_ctrl:1
	s_nop 1
	v_add_f32_dpp v30, v30, v30 row_half_mirror row_mask:0xf bank_mask:0xf bound_ctrl:1
	ds_write_b32 v32, v30 offset:49208
	v_mul_lo_u32 v30, v237, s43
	v_add_u32_e32 v31, v30, v35
	v_add_u32_e32 v30, v30, v34
	buffer_load_dwordx4 v[86:89], v31, s[44:47], 0 offen
	buffer_load_dwordx4 v[92:95], v31, s[44:47], s20 offen
	buffer_load_dwordx4 v[98:101], v31, s[44:47], s21 offen
	buffer_load_dwordx4 v[150:153], v31, s[44:47], s23 offen
	buffer_load_dwordx2 v[90:91], v30, s[44:47], 0 offen
	buffer_load_dwordx2 v[102:103], v30, s[44:47], s33 offen
	buffer_load_dwordx2 v[96:97], v30, s[44:47], s21 offen
	buffer_load_dwordx2 v[154:155], v30, s[44:47], s94 offen
	s_waitcnt vmcnt(27)
	v_mfma_f32_16x16x128_f8f6f4 v[156:159], v[156:161], v[18:23], 0 cbsz:2 blgp:2
	s_waitcnt vmcnt(26)
	v_mfma_f32_16x16x128_f8f6f4 v[156:159], v[168:173], v[12:17], v[156:159] cbsz:2 blgp:2
	s_waitcnt vmcnt(25)
	v_mfma_f32_16x16x128_f8f6f4 v[156:159], v[162:167], v[6:11], v[156:159] cbsz:2 blgp:2
	s_waitcnt vmcnt(24)
	v_mfma_f32_16x16x128_f8f6f4 v[156:159], v[174:179], v[0:5], v[156:159] cbsz:2 blgp:2
	s_nop 7
	v_cndmask_b32_e64 v30, v156, v157, s[4:5]
	v_cndmask_b32_e64 v30, v30, v158, s[2:3]
	v_cndmask_b32_e32 v30, v30, v159, vcc
	v_mul_f32_e32 v31, v33, v30
	s_nop 1
	v_mov_b32_dpp v31, v31 quad_perm:[1,0,3,2] row_mask:0xf bank_mask:0xf bound_ctrl:1
	v_fmac_f32_e32 v31, v33, v30
	s_nop 1
	v_add_f32_dpp v30, v31, v31 quad_perm:[2,3,0,1] row_mask:0xf bank_mask:0xf bound_ctrl:1
	s_nop 1
	v_add_f32_dpp v30, v30, v30 row_half_mirror row_mask:0xf bank_mask:0xf bound_ctrl:1
	ds_write_b32 v32, v30 offset:49212
	v_mul_lo_u32 v30, v238, s43
	v_add_u32_e32 v31, v30, v35
	v_add_u32_e32 v30, v30, v34
	buffer_load_dwordx4 v[156:159], v31, s[44:47], 0 offen
	buffer_load_dwordx4 v[162:165], v31, s[44:47], s20 offen
	buffer_load_dwordx4 v[168:171], v31, s[44:47], s21 offen
	buffer_load_dwordx4 v[174:177], v31, s[44:47], s23 offen
	buffer_load_dwordx2 v[160:161], v30, s[44:47], 0 offen
	buffer_load_dwordx2 v[172:173], v30, s[44:47], s33 offen
	buffer_load_dwordx2 v[166:167], v30, s[44:47], s21 offen
	buffer_load_dwordx2 v[178:179], v30, s[44:47], s94 offen
	s_waitcnt vmcnt(27)
	v_mfma_f32_16x16x128_f8f6f4 v[24:27], v[24:29], v[18:23], 0 cbsz:2 blgp:2
	s_waitcnt vmcnt(26)
	v_mfma_f32_16x16x128_f8f6f4 v[24:27], v[44:49], v[12:17], v[24:27] cbsz:2 blgp:2
	s_waitcnt vmcnt(25)
	v_mfma_f32_16x16x128_f8f6f4 v[24:27], v[38:43], v[6:11], v[24:27] cbsz:2 blgp:2
	s_waitcnt vmcnt(24)
	v_mfma_f32_16x16x128_f8f6f4 v[24:27], v[50:55], v[0:5], v[24:27] cbsz:2 blgp:2
	s_nop 7
	v_cndmask_b32_e64 v24, v24, v25, s[4:5]
	v_cndmask_b32_e64 v24, v24, v26, s[2:3]
	v_cndmask_b32_e32 v24, v24, v27, vcc
	v_mul_f32_e32 v25, v33, v24
	s_nop 1
	v_mov_b32_dpp v25, v25 quad_perm:[1,0,3,2] row_mask:0xf bank_mask:0xf bound_ctrl:1
	v_fmac_f32_e32 v25, v33, v24
	s_nop 1
	v_add_f32_dpp v24, v25, v25 quad_perm:[2,3,0,1] row_mask:0xf bank_mask:0xf bound_ctrl:1
	s_nop 1
	v_add_f32_dpp v24, v24, v24 row_half_mirror row_mask:0xf bank_mask:0xf bound_ctrl:1
	ds_write_b32 v32, v24 offset:49216
	v_mul_lo_u32 v24, v239, s43
	v_add_u32_e32 v28, v24, v35
	v_add_u32_e32 v30, v24, v34
	buffer_load_dwordx4 v[24:27], v28, s[44:47], 0 offen
	buffer_load_dwordx4 v[38:41], v28, s[44:47], s20 offen
	buffer_load_dwordx4 v[44:47], v28, s[44:47], s21 offen
	buffer_load_dwordx4 v[50:53], v28, s[44:47], s23 offen
	s_nop 0
	buffer_load_dwordx2 v[28:29], v30, s[44:47], 0 offen
	buffer_load_dwordx2 v[48:49], v30, s[44:47], s33 offen
	buffer_load_dwordx2 v[42:43], v30, s[44:47], s21 offen
	buffer_load_dwordx2 v[54:55], v30, s[44:47], s94 offen
	s_waitcnt vmcnt(27)
	v_mfma_f32_16x16x128_f8f6f4 v[56:59], v[56:61], v[18:23], 0 cbsz:2 blgp:2
	s_waitcnt vmcnt(26)
	v_mfma_f32_16x16x128_f8f6f4 v[56:59], v[68:73], v[12:17], v[56:59] cbsz:2 blgp:2
	s_waitcnt vmcnt(25)
	v_mfma_f32_16x16x128_f8f6f4 v[56:59], v[62:67], v[6:11], v[56:59] cbsz:2 blgp:2
	s_waitcnt vmcnt(24)
	v_mfma_f32_16x16x128_f8f6f4 v[56:59], v[74:79], v[0:5], v[56:59] cbsz:2 blgp:2
	s_nop 7
	v_cndmask_b32_e64 v30, v56, v57, s[4:5]
	v_cndmask_b32_e64 v30, v30, v58, s[2:3]
	v_cndmask_b32_e32 v30, v30, v59, vcc
	v_mul_f32_e32 v31, v33, v30
	s_nop 1
	v_mov_b32_dpp v31, v31 quad_perm:[1,0,3,2] row_mask:0xf bank_mask:0xf bound_ctrl:1
	v_fmac_f32_e32 v31, v33, v30
	s_nop 1
	v_add_f32_dpp v30, v31, v31 quad_perm:[2,3,0,1] row_mask:0xf bank_mask:0xf bound_ctrl:1
	s_nop 1
	v_add_f32_dpp v30, v30, v30 row_half_mirror row_mask:0xf bank_mask:0xf bound_ctrl:1
	ds_write_b32 v32, v30 offset:49220
	v_mul_lo_u32 v30, v240, s43
	v_add_u32_e32 v31, v30, v35
	v_add_u32_e32 v30, v30, v34
	buffer_load_dwordx4 v[56:59], v31, s[44:47], 0 offen
	buffer_load_dwordx4 v[62:65], v31, s[44:47], s20 offen
	buffer_load_dwordx4 v[68:71], v31, s[44:47], s21 offen
	buffer_load_dwordx4 v[74:77], v31, s[44:47], s23 offen
	buffer_load_dwordx2 v[60:61], v30, s[44:47], 0 offen
	buffer_load_dwordx2 v[72:73], v30, s[44:47], s33 offen
	buffer_load_dwordx2 v[66:67], v30, s[44:47], s21 offen
	buffer_load_dwordx2 v[78:79], v30, s[44:47], s94 offen
	s_waitcnt vmcnt(27)
	v_mfma_f32_16x16x128_f8f6f4 v[86:89], v[86:91], v[18:23], 0 cbsz:2 blgp:2
	s_waitcnt vmcnt(26)
	v_mfma_f32_16x16x128_f8f6f4 v[86:89], v[98:103], v[12:17], v[86:89] cbsz:2 blgp:2
	s_waitcnt vmcnt(25)
	v_mfma_f32_16x16x128_f8f6f4 v[86:89], v[92:97], v[6:11], v[86:89] cbsz:2 blgp:2
	s_waitcnt vmcnt(24)
	v_mfma_f32_16x16x128_f8f6f4 v[86:89], v[150:155], v[0:5], v[86:89] cbsz:2 blgp:2
	s_nop 7
	v_cndmask_b32_e64 v30, v86, v87, s[4:5]
	v_cndmask_b32_e64 v30, v30, v88, s[2:3]
	v_cndmask_b32_e32 v30, v30, v89, vcc
	v_mul_f32_e32 v31, v33, v30
	s_nop 1
	v_mov_b32_dpp v31, v31 quad_perm:[1,0,3,2] row_mask:0xf bank_mask:0xf bound_ctrl:1
	v_fmac_f32_e32 v31, v33, v30
	s_nop 1
	v_add_f32_dpp v30, v31, v31 quad_perm:[2,3,0,1] row_mask:0xf bank_mask:0xf bound_ctrl:1
	s_nop 1
	v_add_f32_dpp v30, v30, v30 row_half_mirror row_mask:0xf bank_mask:0xf bound_ctrl:1
	ds_write_b32 v32, v30 offset:49224
	v_mul_lo_u32 v30, v241, s43
	v_add_u32_e32 v31, v30, v35
	v_add_u32_e32 v30, v30, v34
	buffer_load_dwordx4 v[86:89], v31, s[44:47], 0 offen
	buffer_load_dwordx4 v[92:95], v31, s[44:47], s20 offen
	buffer_load_dwordx4 v[98:101], v31, s[44:47], s21 offen
	buffer_load_dwordx4 v[150:153], v31, s[44:47], s23 offen
	buffer_load_dwordx2 v[90:91], v30, s[44:47], 0 offen
	buffer_load_dwordx2 v[102:103], v30, s[44:47], s33 offen
	buffer_load_dwordx2 v[96:97], v30, s[44:47], s21 offen
	buffer_load_dwordx2 v[154:155], v30, s[44:47], s94 offen
	s_waitcnt vmcnt(27)
	v_mfma_f32_16x16x128_f8f6f4 v[156:159], v[156:161], v[18:23], 0 cbsz:2 blgp:2
	s_waitcnt vmcnt(26)
	v_mfma_f32_16x16x128_f8f6f4 v[156:159], v[168:173], v[12:17], v[156:159] cbsz:2 blgp:2
	s_waitcnt vmcnt(25)
	v_mfma_f32_16x16x128_f8f6f4 v[156:159], v[162:167], v[6:11], v[156:159] cbsz:2 blgp:2
	s_waitcnt vmcnt(24)
	v_mfma_f32_16x16x128_f8f6f4 v[156:159], v[174:179], v[0:5], v[156:159] cbsz:2 blgp:2
	s_nop 7
	v_cndmask_b32_e64 v30, v156, v157, s[4:5]
	v_cndmask_b32_e64 v30, v30, v158, s[2:3]
	v_cndmask_b32_e32 v30, v30, v159, vcc
	v_mul_f32_e32 v31, v33, v30
	s_nop 1
	v_mov_b32_dpp v31, v31 quad_perm:[1,0,3,2] row_mask:0xf bank_mask:0xf bound_ctrl:1
	v_fmac_f32_e32 v31, v33, v30
	s_nop 1
	v_add_f32_dpp v30, v31, v31 quad_perm:[2,3,0,1] row_mask:0xf bank_mask:0xf bound_ctrl:1
	s_nop 1
	v_add_f32_dpp v30, v30, v30 row_half_mirror row_mask:0xf bank_mask:0xf bound_ctrl:1
	ds_write_b32 v32, v30 offset:49228
	v_mul_lo_u32 v30, v242, s43
	v_add_u32_e32 v31, v30, v35
	v_add_u32_e32 v30, v30, v34
	buffer_load_dwordx4 v[156:159], v31, s[44:47], 0 offen
	buffer_load_dwordx4 v[162:165], v31, s[44:47], s20 offen
	buffer_load_dwordx4 v[168:171], v31, s[44:47], s21 offen
	buffer_load_dwordx4 v[174:177], v31, s[44:47], s23 offen
	buffer_load_dwordx2 v[160:161], v30, s[44:47], 0 offen
	buffer_load_dwordx2 v[172:173], v30, s[44:47], s33 offen
	buffer_load_dwordx2 v[166:167], v30, s[44:47], s21 offen
	buffer_load_dwordx2 v[178:179], v30, s[44:47], s94 offen
	s_waitcnt vmcnt(27)
	v_mfma_f32_16x16x128_f8f6f4 v[24:27], v[24:29], v[18:23], 0 cbsz:2 blgp:2
	s_waitcnt vmcnt(26)
	v_mfma_f32_16x16x128_f8f6f4 v[24:27], v[44:49], v[12:17], v[24:27] cbsz:2 blgp:2
	s_waitcnt vmcnt(25)
	v_mfma_f32_16x16x128_f8f6f4 v[24:27], v[38:43], v[6:11], v[24:27] cbsz:2 blgp:2
	s_waitcnt vmcnt(24)
	v_mfma_f32_16x16x128_f8f6f4 v[24:27], v[50:55], v[0:5], v[24:27] cbsz:2 blgp:2
	s_nop 7
	v_cndmask_b32_e64 v24, v24, v25, s[4:5]
	v_cndmask_b32_e64 v24, v24, v26, s[2:3]
	v_cndmask_b32_e32 v24, v24, v27, vcc
	v_mul_f32_e32 v25, v33, v24
	s_nop 1
	v_mov_b32_dpp v25, v25 quad_perm:[1,0,3,2] row_mask:0xf bank_mask:0xf bound_ctrl:1
	v_fmac_f32_e32 v25, v33, v24
	s_nop 1
	v_add_f32_dpp v24, v25, v25 quad_perm:[2,3,0,1] row_mask:0xf bank_mask:0xf bound_ctrl:1
	s_nop 1
	v_add_f32_dpp v24, v24, v24 row_half_mirror row_mask:0xf bank_mask:0xf bound_ctrl:1
	ds_write_b32 v32, v24 offset:49232
	v_mul_lo_u32 v24, v243, s43
	v_add_u32_e32 v28, v24, v35
	v_add_u32_e32 v30, v24, v34
	buffer_load_dwordx4 v[24:27], v28, s[44:47], 0 offen
	buffer_load_dwordx4 v[38:41], v28, s[44:47], s20 offen
	buffer_load_dwordx4 v[44:47], v28, s[44:47], s21 offen
	buffer_load_dwordx4 v[50:53], v28, s[44:47], s23 offen
	s_nop 0
	buffer_load_dwordx2 v[28:29], v30, s[44:47], 0 offen
	buffer_load_dwordx2 v[48:49], v30, s[44:47], s33 offen
	buffer_load_dwordx2 v[42:43], v30, s[44:47], s21 offen
	buffer_load_dwordx2 v[54:55], v30, s[44:47], s94 offen
	s_waitcnt vmcnt(27)
	v_mfma_f32_16x16x128_f8f6f4 v[56:59], v[56:61], v[18:23], 0 cbsz:2 blgp:2
	s_waitcnt vmcnt(26)
	v_mfma_f32_16x16x128_f8f6f4 v[56:59], v[68:73], v[12:17], v[56:59] cbsz:2 blgp:2
	s_waitcnt vmcnt(25)
	v_mfma_f32_16x16x128_f8f6f4 v[56:59], v[62:67], v[6:11], v[56:59] cbsz:2 blgp:2
	s_waitcnt vmcnt(24)
	v_mfma_f32_16x16x128_f8f6f4 v[56:59], v[74:79], v[0:5], v[56:59] cbsz:2 blgp:2
	s_nop 7
	v_cndmask_b32_e64 v30, v56, v57, s[4:5]
	v_cndmask_b32_e64 v30, v30, v58, s[2:3]
	v_cndmask_b32_e32 v30, v30, v59, vcc
	v_mul_f32_e32 v31, v33, v30
	s_nop 1
	v_mov_b32_dpp v31, v31 quad_perm:[1,0,3,2] row_mask:0xf bank_mask:0xf bound_ctrl:1
	v_fmac_f32_e32 v31, v33, v30
	s_nop 1
	v_add_f32_dpp v30, v31, v31 quad_perm:[2,3,0,1] row_mask:0xf bank_mask:0xf bound_ctrl:1
	s_nop 1
	v_add_f32_dpp v30, v30, v30 row_half_mirror row_mask:0xf bank_mask:0xf bound_ctrl:1
	ds_write_b32 v32, v30 offset:49236
	v_mul_lo_u32 v30, v244, s43
	v_add_u32_e32 v31, v30, v35
	v_add_u32_e32 v30, v30, v34
	buffer_load_dwordx4 v[56:59], v31, s[44:47], 0 offen
	buffer_load_dwordx4 v[62:65], v31, s[44:47], s20 offen
	buffer_load_dwordx4 v[68:71], v31, s[44:47], s21 offen
	buffer_load_dwordx4 v[74:77], v31, s[44:47], s23 offen
	buffer_load_dwordx2 v[60:61], v30, s[44:47], 0 offen
	buffer_load_dwordx2 v[72:73], v30, s[44:47], s33 offen
	buffer_load_dwordx2 v[66:67], v30, s[44:47], s21 offen
	buffer_load_dwordx2 v[78:79], v30, s[44:47], s94 offen
	s_waitcnt vmcnt(27)
	v_mfma_f32_16x16x128_f8f6f4 v[86:89], v[86:91], v[18:23], 0 cbsz:2 blgp:2
	s_waitcnt vmcnt(26)
	v_mfma_f32_16x16x128_f8f6f4 v[86:89], v[98:103], v[12:17], v[86:89] cbsz:2 blgp:2
	s_waitcnt vmcnt(25)
	v_mfma_f32_16x16x128_f8f6f4 v[86:89], v[92:97], v[6:11], v[86:89] cbsz:2 blgp:2
	s_waitcnt vmcnt(24)
	v_mfma_f32_16x16x128_f8f6f4 v[86:89], v[150:155], v[0:5], v[86:89] cbsz:2 blgp:2
	s_nop 7
	v_cndmask_b32_e64 v30, v86, v87, s[4:5]
	v_cndmask_b32_e64 v30, v30, v88, s[2:3]
	v_cndmask_b32_e32 v30, v30, v89, vcc
	v_mul_f32_e32 v31, v33, v30
	s_nop 1
	v_mov_b32_dpp v31, v31 quad_perm:[1,0,3,2] row_mask:0xf bank_mask:0xf bound_ctrl:1
	v_fmac_f32_e32 v31, v33, v30
	s_nop 1
	v_add_f32_dpp v30, v31, v31 quad_perm:[2,3,0,1] row_mask:0xf bank_mask:0xf bound_ctrl:1
	s_nop 1
	v_add_f32_dpp v30, v30, v30 row_half_mirror row_mask:0xf bank_mask:0xf bound_ctrl:1
	ds_write_b32 v32, v30 offset:49240
	v_mul_lo_u32 v30, v245, s43
	v_add_u32_e32 v31, v30, v35
	v_add_u32_e32 v30, v30, v34
	buffer_load_dwordx4 v[86:89], v31, s[44:47], 0 offen
	buffer_load_dwordx4 v[92:95], v31, s[44:47], s20 offen
	buffer_load_dwordx4 v[98:101], v31, s[44:47], s21 offen
	buffer_load_dwordx4 v[150:153], v31, s[44:47], s23 offen
	buffer_load_dwordx2 v[90:91], v30, s[44:47], 0 offen
	buffer_load_dwordx2 v[102:103], v30, s[44:47], s33 offen
	buffer_load_dwordx2 v[96:97], v30, s[44:47], s21 offen
	buffer_load_dwordx2 v[154:155], v30, s[44:47], s94 offen
	s_waitcnt vmcnt(27)
	v_mfma_f32_16x16x128_f8f6f4 v[156:159], v[156:161], v[18:23], 0 cbsz:2 blgp:2
	s_waitcnt vmcnt(26)
	v_mfma_f32_16x16x128_f8f6f4 v[156:159], v[168:173], v[12:17], v[156:159] cbsz:2 blgp:2
	s_waitcnt vmcnt(25)
	v_mfma_f32_16x16x128_f8f6f4 v[156:159], v[162:167], v[6:11], v[156:159] cbsz:2 blgp:2
	s_waitcnt vmcnt(24)
	v_mfma_f32_16x16x128_f8f6f4 v[156:159], v[174:179], v[0:5], v[156:159] cbsz:2 blgp:2
	s_nop 7
	v_cndmask_b32_e64 v30, v156, v157, s[4:5]
	v_cndmask_b32_e64 v30, v30, v158, s[2:3]
	v_cndmask_b32_e32 v30, v30, v159, vcc
	v_mul_f32_e32 v31, v33, v30
	s_nop 1
	v_mov_b32_dpp v31, v31 quad_perm:[1,0,3,2] row_mask:0xf bank_mask:0xf bound_ctrl:1
	v_fmac_f32_e32 v31, v33, v30
	s_nop 1
	v_add_f32_dpp v30, v31, v31 quad_perm:[2,3,0,1] row_mask:0xf bank_mask:0xf bound_ctrl:1
	s_nop 1
	v_add_f32_dpp v30, v30, v30 row_half_mirror row_mask:0xf bank_mask:0xf bound_ctrl:1
	ds_write_b32 v32, v30 offset:49244
	v_mul_lo_u32 v30, v246, s43
	v_add_u32_e32 v31, v30, v35
	v_add_u32_e32 v30, v30, v34
	buffer_load_dwordx4 v[156:159], v31, s[44:47], 0 offen
	buffer_load_dwordx4 v[162:165], v31, s[44:47], s20 offen
	buffer_load_dwordx4 v[168:171], v31, s[44:47], s21 offen
	buffer_load_dwordx4 v[174:177], v31, s[44:47], s23 offen
	buffer_load_dwordx2 v[160:161], v30, s[44:47], 0 offen
	buffer_load_dwordx2 v[172:173], v30, s[44:47], s33 offen
	buffer_load_dwordx2 v[166:167], v30, s[44:47], s21 offen
	buffer_load_dwordx2 v[178:179], v30, s[44:47], s94 offen
	s_waitcnt vmcnt(27)
	v_mfma_f32_16x16x128_f8f6f4 v[24:27], v[24:29], v[18:23], 0 cbsz:2 blgp:2
	s_waitcnt vmcnt(26)
	v_mfma_f32_16x16x128_f8f6f4 v[24:27], v[44:49], v[12:17], v[24:27] cbsz:2 blgp:2
	s_waitcnt vmcnt(25)
	v_mfma_f32_16x16x128_f8f6f4 v[24:27], v[38:43], v[6:11], v[24:27] cbsz:2 blgp:2
	s_waitcnt vmcnt(24)
	v_mfma_f32_16x16x128_f8f6f4 v[24:27], v[50:55], v[0:5], v[24:27] cbsz:2 blgp:2
	s_nop 7
	v_cndmask_b32_e64 v24, v24, v25, s[4:5]
	v_cndmask_b32_e64 v24, v24, v26, s[2:3]
	v_cndmask_b32_e32 v24, v24, v27, vcc
	v_mul_f32_e32 v25, v33, v24
	s_nop 1
	v_mov_b32_dpp v25, v25 quad_perm:[1,0,3,2] row_mask:0xf bank_mask:0xf bound_ctrl:1
	v_fmac_f32_e32 v25, v33, v24
	s_nop 1
	v_add_f32_dpp v24, v25, v25 quad_perm:[2,3,0,1] row_mask:0xf bank_mask:0xf bound_ctrl:1
	s_nop 1
	v_add_f32_dpp v24, v24, v24 row_half_mirror row_mask:0xf bank_mask:0xf bound_ctrl:1
	ds_write_b32 v32, v24 offset:49248
	v_mul_lo_u32 v24, v247, s43
	v_add_u32_e32 v28, v24, v35
	v_add_u32_e32 v30, v24, v34
	buffer_load_dwordx4 v[24:27], v28, s[44:47], 0 offen
	buffer_load_dwordx4 v[38:41], v28, s[44:47], s20 offen
	buffer_load_dwordx4 v[44:47], v28, s[44:47], s21 offen
	buffer_load_dwordx4 v[50:53], v28, s[44:47], s23 offen
	s_nop 0
	buffer_load_dwordx2 v[28:29], v30, s[44:47], 0 offen
	buffer_load_dwordx2 v[48:49], v30, s[44:47], s33 offen
	buffer_load_dwordx2 v[42:43], v30, s[44:47], s21 offen
	buffer_load_dwordx2 v[54:55], v30, s[44:47], s94 offen
	s_waitcnt vmcnt(27)
	v_mfma_f32_16x16x128_f8f6f4 v[56:59], v[56:61], v[18:23], 0 cbsz:2 blgp:2
	s_waitcnt vmcnt(26)
	v_mfma_f32_16x16x128_f8f6f4 v[56:59], v[68:73], v[12:17], v[56:59] cbsz:2 blgp:2
	s_waitcnt vmcnt(25)
	v_mfma_f32_16x16x128_f8f6f4 v[56:59], v[62:67], v[6:11], v[56:59] cbsz:2 blgp:2
	s_waitcnt vmcnt(24)
	v_mfma_f32_16x16x128_f8f6f4 v[56:59], v[74:79], v[0:5], v[56:59] cbsz:2 blgp:2
	s_nop 7
	v_cndmask_b32_e64 v30, v56, v57, s[4:5]
	v_cndmask_b32_e64 v30, v30, v58, s[2:3]
	v_cndmask_b32_e32 v30, v30, v59, vcc
	v_mul_f32_e32 v31, v33, v30
	s_nop 1
	v_mov_b32_dpp v31, v31 quad_perm:[1,0,3,2] row_mask:0xf bank_mask:0xf bound_ctrl:1
	v_fmac_f32_e32 v31, v33, v30
	s_nop 1
	v_add_f32_dpp v30, v31, v31 quad_perm:[2,3,0,1] row_mask:0xf bank_mask:0xf bound_ctrl:1
	s_nop 1
	v_add_f32_dpp v30, v30, v30 row_half_mirror row_mask:0xf bank_mask:0xf bound_ctrl:1
	ds_write_b32 v32, v30 offset:49252
	v_mul_lo_u32 v30, v248, s43
	v_add_u32_e32 v31, v30, v35
	v_add_u32_e32 v30, v30, v34
	buffer_load_dwordx4 v[56:59], v31, s[44:47], 0 offen
	buffer_load_dwordx4 v[62:65], v31, s[44:47], s20 offen
	buffer_load_dwordx4 v[68:71], v31, s[44:47], s21 offen
	buffer_load_dwordx4 v[74:77], v31, s[44:47], s23 offen
	buffer_load_dwordx2 v[60:61], v30, s[44:47], 0 offen
	buffer_load_dwordx2 v[72:73], v30, s[44:47], s33 offen
	buffer_load_dwordx2 v[66:67], v30, s[44:47], s21 offen
	buffer_load_dwordx2 v[78:79], v30, s[44:47], s94 offen
	s_waitcnt vmcnt(27)
	v_mfma_f32_16x16x128_f8f6f4 v[86:89], v[86:91], v[18:23], 0 cbsz:2 blgp:2
	s_waitcnt vmcnt(26)
	v_mfma_f32_16x16x128_f8f6f4 v[86:89], v[98:103], v[12:17], v[86:89] cbsz:2 blgp:2
	s_waitcnt vmcnt(25)
	v_mfma_f32_16x16x128_f8f6f4 v[86:89], v[92:97], v[6:11], v[86:89] cbsz:2 blgp:2
	s_waitcnt vmcnt(24)
	v_mfma_f32_16x16x128_f8f6f4 v[86:89], v[150:155], v[0:5], v[86:89] cbsz:2 blgp:2
	s_nop 7
	v_cndmask_b32_e64 v30, v86, v87, s[4:5]
	v_cndmask_b32_e64 v30, v30, v88, s[2:3]
	v_cndmask_b32_e32 v30, v30, v89, vcc
	v_mul_f32_e32 v31, v33, v30
	s_nop 1
	v_mov_b32_dpp v31, v31 quad_perm:[1,0,3,2] row_mask:0xf bank_mask:0xf bound_ctrl:1
	v_fmac_f32_e32 v31, v33, v30
	s_nop 1
	v_add_f32_dpp v30, v31, v31 quad_perm:[2,3,0,1] row_mask:0xf bank_mask:0xf bound_ctrl:1
	s_nop 1
	v_add_f32_dpp v30, v30, v30 row_half_mirror row_mask:0xf bank_mask:0xf bound_ctrl:1
	ds_write_b32 v32, v30 offset:49256
	v_mul_lo_u32 v30, v249, s43
	v_add_u32_e32 v31, v30, v35
	v_add_u32_e32 v30, v30, v34
	buffer_load_dwordx4 v[86:89], v31, s[44:47], 0 offen
	buffer_load_dwordx4 v[92:95], v31, s[44:47], s20 offen
	buffer_load_dwordx4 v[98:101], v31, s[44:47], s21 offen
	buffer_load_dwordx4 v[150:153], v31, s[44:47], s23 offen
	buffer_load_dwordx2 v[90:91], v30, s[44:47], 0 offen
	buffer_load_dwordx2 v[102:103], v30, s[44:47], s33 offen
	buffer_load_dwordx2 v[96:97], v30, s[44:47], s21 offen
	buffer_load_dwordx2 v[154:155], v30, s[44:47], s94 offen
	s_waitcnt vmcnt(27)
	v_mfma_f32_16x16x128_f8f6f4 v[156:159], v[156:161], v[18:23], 0 cbsz:2 blgp:2
	s_waitcnt vmcnt(26)
	v_mfma_f32_16x16x128_f8f6f4 v[156:159], v[168:173], v[12:17], v[156:159] cbsz:2 blgp:2
	s_waitcnt vmcnt(25)
	v_mfma_f32_16x16x128_f8f6f4 v[156:159], v[162:167], v[6:11], v[156:159] cbsz:2 blgp:2
	s_waitcnt vmcnt(24)
	v_mfma_f32_16x16x128_f8f6f4 v[156:159], v[174:179], v[0:5], v[156:159] cbsz:2 blgp:2
	s_nop 7
	v_cndmask_b32_e64 v30, v156, v157, s[4:5]
	v_cndmask_b32_e64 v30, v30, v158, s[2:3]
	v_cndmask_b32_e32 v30, v30, v159, vcc
	v_mul_f32_e32 v31, v33, v30
	s_nop 1
	v_mov_b32_dpp v31, v31 quad_perm:[1,0,3,2] row_mask:0xf bank_mask:0xf bound_ctrl:1
	v_fmac_f32_e32 v31, v33, v30
	s_nop 1
	v_add_f32_dpp v30, v31, v31 quad_perm:[2,3,0,1] row_mask:0xf bank_mask:0xf bound_ctrl:1
	s_nop 1
	v_add_f32_dpp v30, v30, v30 row_half_mirror row_mask:0xf bank_mask:0xf bound_ctrl:1
	ds_write_b32 v32, v30 offset:49260
	ds_bpermute_b32 v30, v36, v128 offset:240
	s_waitcnt lgkmcnt(0)
	v_mul_lo_u32 v30, v30, s43
	v_add_u32_e32 v31, v30, v35
	v_add_u32_e32 v30, v30, v34
	buffer_load_dwordx4 v[156:159], v31, s[44:47], 0 offen
	buffer_load_dwordx4 v[162:165], v31, s[44:47], s20 offen
	buffer_load_dwordx4 v[168:171], v31, s[44:47], s21 offen
	buffer_load_dwordx4 v[174:177], v31, s[44:47], s23 offen
	buffer_load_dwordx2 v[160:161], v30, s[44:47], 0 offen
	buffer_load_dwordx2 v[172:173], v30, s[44:47], s33 offen
	buffer_load_dwordx2 v[166:167], v30, s[44:47], s21 offen
	buffer_load_dwordx2 v[178:179], v30, s[44:47], s94 offen
	s_waitcnt vmcnt(27)
	v_mfma_f32_16x16x128_f8f6f4 v[24:27], v[24:29], v[18:23], 0 cbsz:2 blgp:2
	s_waitcnt vmcnt(26)
	v_mfma_f32_16x16x128_f8f6f4 v[24:27], v[44:49], v[12:17], v[24:27] cbsz:2 blgp:2
	s_waitcnt vmcnt(25)
	v_mfma_f32_16x16x128_f8f6f4 v[24:27], v[38:43], v[6:11], v[24:27] cbsz:2 blgp:2
	s_waitcnt vmcnt(24)
	v_mfma_f32_16x16x128_f8f6f4 v[24:27], v[50:55], v[0:5], v[24:27] cbsz:2 blgp:2
	s_nop 7
	v_cndmask_b32_e64 v24, v24, v25, s[4:5]
	v_cndmask_b32_e64 v24, v24, v26, s[2:3]
	v_cndmask_b32_e32 v24, v24, v27, vcc
	v_mul_f32_e32 v25, v33, v24
	s_nop 1
	v_mov_b32_dpp v25, v25 quad_perm:[1,0,3,2] row_mask:0xf bank_mask:0xf bound_ctrl:1
	v_fmac_f32_e32 v25, v33, v24
	s_nop 1
	v_add_f32_dpp v24, v25, v25 quad_perm:[2,3,0,1] row_mask:0xf bank_mask:0xf bound_ctrl:1
	s_nop 1
	v_add_f32_dpp v24, v24, v24 row_half_mirror row_mask:0xf bank_mask:0xf bound_ctrl:1
	ds_write_b32 v32, v24 offset:49264
	s_waitcnt vmcnt(19)
	v_mfma_f32_16x16x128_f8f6f4 v[24:27], v[56:61], v[18:23], 0 cbsz:2 blgp:2
	s_waitcnt vmcnt(18)
	v_mfma_f32_16x16x128_f8f6f4 v[24:27], v[68:73], v[12:17], v[24:27] cbsz:2 blgp:2
	s_waitcnt vmcnt(17)
	v_mfma_f32_16x16x128_f8f6f4 v[24:27], v[62:67], v[6:11], v[24:27] cbsz:2 blgp:2
	s_waitcnt vmcnt(16)
	v_mfma_f32_16x16x128_f8f6f4 v[24:27], v[74:79], v[0:5], v[24:27] cbsz:2 blgp:2
	s_nop 7
	v_cndmask_b32_e64 v24, v24, v25, s[4:5]
	v_cndmask_b32_e64 v24, v24, v26, s[2:3]
	v_cndmask_b32_e32 v24, v24, v27, vcc
	v_mul_f32_e32 v25, v33, v24
	s_nop 1
	v_mov_b32_dpp v25, v25 quad_perm:[1,0,3,2] row_mask:0xf bank_mask:0xf bound_ctrl:1
	v_fmac_f32_e32 v25, v33, v24
	s_nop 1
	v_add_f32_dpp v24, v25, v25 quad_perm:[2,3,0,1] row_mask:0xf bank_mask:0xf bound_ctrl:1
	s_nop 1
	v_add_f32_dpp v24, v24, v24 row_half_mirror row_mask:0xf bank_mask:0xf bound_ctrl:1
	ds_write_b32 v32, v24 offset:49268
	s_waitcnt vmcnt(11)
	v_mfma_f32_16x16x128_f8f6f4 v[24:27], v[86:91], v[18:23], 0 cbsz:2 blgp:2
	s_waitcnt vmcnt(10)
	v_mfma_f32_16x16x128_f8f6f4 v[24:27], v[98:103], v[12:17], v[24:27] cbsz:2 blgp:2
	s_waitcnt vmcnt(9)
	v_mfma_f32_16x16x128_f8f6f4 v[24:27], v[92:97], v[6:11], v[24:27] cbsz:2 blgp:2
	s_waitcnt vmcnt(8)
	v_mfma_f32_16x16x128_f8f6f4 v[24:27], v[150:155], v[0:5], v[24:27] cbsz:2 blgp:2
	s_nop 7
	v_cndmask_b32_e64 v24, v24, v25, s[4:5]
	v_cndmask_b32_e64 v24, v24, v26, s[2:3]
	v_cndmask_b32_e32 v24, v24, v27, vcc
	v_mul_f32_e32 v25, v33, v24
	s_nop 1
	v_mov_b32_dpp v25, v25 quad_perm:[1,0,3,2] row_mask:0xf bank_mask:0xf bound_ctrl:1
	v_fmac_f32_e32 v25, v33, v24
	s_nop 1
	v_add_f32_dpp v24, v25, v25 quad_perm:[2,3,0,1] row_mask:0xf bank_mask:0xf bound_ctrl:1
	s_nop 1
	v_add_f32_dpp v24, v24, v24 row_half_mirror row_mask:0xf bank_mask:0xf bound_ctrl:1
	ds_write_b32 v32, v24 offset:49272
	s_waitcnt vmcnt(3)
	v_mfma_f32_16x16x128_f8f6f4 v[18:21], v[156:161], v[18:23], 0 cbsz:2 blgp:2
	s_waitcnt vmcnt(2)
	v_mfma_f32_16x16x128_f8f6f4 v[12:15], v[168:173], v[12:17], v[18:21] cbsz:2 blgp:2
	s_waitcnt vmcnt(1)
	v_mfma_f32_16x16x128_f8f6f4 v[6:9], v[162:167], v[6:11], v[12:15] cbsz:2 blgp:2
	s_waitcnt vmcnt(0)
	v_mfma_f32_16x16x128_f8f6f4 v[0:3], v[174:179], v[0:5], v[6:9] cbsz:2 blgp:2
	s_nop 7
	v_cndmask_b32_e64 v0, v0, v1, s[4:5]
	v_cndmask_b32_e64 v0, v0, v2, s[2:3]
	v_cndmask_b32_e32 v0, v0, v3, vcc
	v_mul_f32_e32 v1, v33, v0
	s_nop 1
	v_mov_b32_dpp v1, v1 quad_perm:[1,0,3,2] row_mask:0xf bank_mask:0xf bound_ctrl:1
	v_fmac_f32_e32 v1, v33, v0
	s_nop 1
	v_add_f32_dpp v0, v1, v1 quad_perm:[2,3,0,1] row_mask:0xf bank_mask:0xf bound_ctrl:1
	s_nop 1
	v_add_f32_dpp v0, v0, v0 row_half_mirror row_mask:0xf bank_mask:0xf bound_ctrl:1
	ds_write_b32 v32, v0 offset:49276
	v_readlane_b32 s1, v130, 0
	s_mulk_i32 s1, 0x600
	s_add_i32 s1, s1, 0x8000000
	v_lshrrev_b32_e32 v0, 1, v129
	s_nop 1
	buffer_load_dwordx4 v[74:77], v129, s[44:47], s1 offen
	buffer_load_dwordx2 v[78:79], v0, s[44:47], s1 offen offset:1024
	v_readlane_b32 s1, v130, 1
	s_mulk_i32 s1, 0x600
	s_add_i32 s1, s1, 0x8000000
	s_nop 2
	buffer_load_dwordx4 v[68:71], v129, s[44:47], s1 offen
	buffer_load_dwordx2 v[72:73], v0, s[44:47], s1 offen offset:1024
	v_readlane_b32 s1, v130, 2
	s_mulk_i32 s1, 0x600
	s_add_i32 s1, s1, 0x8000000
	s_nop 2
	buffer_load_dwordx4 v[56:59], v129, s[44:47], s1 offen
	buffer_load_dwordx2 v[60:61], v0, s[44:47], s1 offen offset:1024
	v_readlane_b32 s1, v130, 3
	s_mulk_i32 s1, 0x600
	s_add_i32 s1, s1, 0x8000000
	s_nop 2
	buffer_load_dwordx4 v[44:47], v129, s[44:47], s1 offen
	buffer_load_dwordx2 v[48:49], v0, s[44:47], s1 offen offset:1024
	v_add_u32_e32 v210, 0x400, v0
	v_readlane_b32 s1, v130, 4
	s_mulk_i32 s1, 0x600
	s_add_i32 s1, s1, 0x8000000
	s_nop 2
	buffer_load_dwordx4 v[62:65], v129, s[44:47], s1 offen
	buffer_load_dwordx2 v[66:67], v0, s[44:47], s1 offen offset:1024
	v_readlane_b32 s1, v130, 5
	s_mulk_i32 s1, 0x600
	s_add_i32 s1, s1, 0x8000000
	s_nop 2
	buffer_load_dwordx4 v[50:53], v129, s[44:47], s1 offen
	buffer_load_dwordx2 v[54:55], v0, s[44:47], s1 offen offset:1024
	v_readlane_b32 s1, v130, 6
	s_mulk_i32 s1, 0x600
	s_add_i32 s1, s1, 0x8000000
	s_nop 2
	buffer_load_dwordx4 v[38:41], v129, s[44:47], s1 offen
	buffer_load_dwordx2 v[42:43], v0, s[44:47], s1 offen offset:1024
	v_readlane_b32 s1, v130, 7
	s_mulk_i32 s1, 0x600
	s_add_i32 s1, s1, 0x8000000
	s_nop 2
	buffer_load_dwordx4 v[32:35], v129, s[44:47], s1 offen
	buffer_load_dwordx2 v[36:37], v0, s[44:47], s1 offen offset:1024
	v_div_scale_f32 v2, s[2:3], v80, v80, 1.0
	v_rcp_f32_e32 v3, v2
	v_div_scale_f32 v4, vcc, 1.0, v80, 1.0
	v_and_b32_e32 v1, -4, v148
	v_fma_f32 v0, -v2, v3, 1.0
	v_fmac_f32_e32 v3, v0, v3
	v_mul_f32_e32 v5, v4, v3
	v_fma_f32 v0, -v2, v5, v4
	v_fmac_f32_e32 v5, v0, v3
	v_lshlrev_b32_e32 v0, 7, v148
	v_and_b32_e32 v0, 0x180, v0
	v_add3_u32 v0, v111, v0, v1
	v_add_u32_e32 v0, 0xc000, v0
	ds_read2_b32 v[0:1], v0 offset1:16
	v_fma_f32 v2, -v2, v5, v4
	v_div_fmas_f32 v2, v2, v3, v5
	v_div_fixup_f32 v2, v2, v80, 1.0
	s_mov_b32 s1, 0x3e6d3388
	s_waitcnt lgkmcnt(0)
	v_mul_f32_e32 v0, v2, v0
	v_mul_f32_e32 v0, v83, v0
	v_fma_f32 v3, |v0|, s1, 1.0
	v_rcp_f32_e32 v3, v3
	v_mul_f32_e32 v5, v0, v0
	v_mul_f32_e32 v5, 0xbf38aa3b, v5
	v_exp_f32_e32 v5, v5
	v_fmamk_f32 v4, v3, 0x3f07dc22, v184
	v_fmaak_f32 v4, v3, v4, 0x3f35f0e3
	v_fmaak_f32 v4, v3, v4, 0xbe11a98e
	v_mul_f32_e32 v1, v2, v1
	v_fmaak_f32 v4, v3, v4, 0x3e027906
	v_mul_f32_e32 v3, v3, v4
	v_mul_f32_e32 v1, v82, v1
	v_mul_f32_e32 v3, v5, v3
	v_fma_f32 v5, |v1|, s1, 1.0
	v_rcp_f32_e32 v5, v5
	v_mul_f32_e32 v4, v0, v3
	v_fma_f32 v3, -v0, v3, v0
	v_cmp_gt_f32_e32 vcc, 0, v0
	v_mul_f32_e32 v2, v206, v84
	v_mov_b32_e32 v180, 0
	v_cndmask_b32_e32 v0, v3, v4, vcc
	v_mul_f32_e32 v211, v2, v0
	v_mul_f32_e32 v2, v1, v1
	v_fmamk_f32 v0, v5, 0x3f07dc22, v184
	v_mul_f32_e32 v2, 0xbf38aa3b, v2
	v_fmaak_f32 v0, v5, v0, 0x3f35f0e3
	v_exp_f32_e32 v2, v2
	v_fmaak_f32 v0, v5, v0, 0xbe11a98e
	v_fmaak_f32 v0, v5, v0, 0x3e027906
	v_mul_f32_e32 v0, v5, v0
	v_mul_f32_e32 v0, v2, v0
	v_mul_f32_e32 v2, v1, v0
	v_fma_f32 v0, -v1, v0, v1
	v_cmp_gt_f32_e32 vcc, 0, v1
	v_mul_f32_e32 v1, v205, v81
	v_mov_b32_e32 v181, v180
	v_cndmask_b32_e32 v0, v0, v2, vcc
	v_mul_f32_e32 v131, v1, v0
	v_mov_b32_e32 v178, v180
	v_mov_b32_e32 v179, v180
	v_mov_b32_e32 v176, v180
	v_mov_b32_e32 v177, v180
	v_mov_b32_e32 v174, v180
	v_mov_b32_e32 v175, v180
	v_mov_b32_e32 v172, v180
	v_mov_b32_e32 v173, v180
	v_mov_b32_e32 v170, v180
	v_mov_b32_e32 v171, v180
	v_mov_b32_e32 v168, v180
	v_mov_b32_e32 v169, v180
	v_mov_b32_e32 v166, v180
	v_mov_b32_e32 v167, v180
	v_mov_b32_e32 v164, v180
	v_mov_b32_e32 v165, v180
	v_mov_b32_e32 v162, v180
	v_mov_b32_e32 v163, v180
	v_mov_b32_e32 v160, v180
	v_mov_b32_e32 v161, v180
	v_mov_b32_e32 v158, v180
	v_mov_b32_e32 v159, v180
	v_mov_b32_e32 v156, v180
	v_mov_b32_e32 v157, v180
	v_mov_b32_e32 v154, v180
	v_mov_b32_e32 v155, v180
	v_mov_b32_e32 v152, v180
	v_mov_b32_e32 v153, v180
	v_mov_b32_e32 v150, v180
	v_mov_b32_e32 v151, v180
